# speedup vs baseline: 1.0006x; 1.0006x over previous
.LBB6_9:
	s_mov_b32 s60, s14
	s_mov_b32 s61, s15
	s_mov_b32 s24, s60
	s_mov_b32 s25, s61
	s_load_dwordx2 s[28:29], s[0:1], 0x58
	s_load_dwordx2 s[30:31], s[0:1], 0x68
	s_load_dwordx2 s[32:33], s[0:1], 0x78
	v_and_b32_e32 v66, 63, v0
	v_lshrrev_b32_e32 v67, 6, v0
	v_and_b32_e32 v68, 15, v0
	v_bfe_u32 v69, v0, 4, 2
	v_mul_u32_u24_e32 v70, 0x2000, v67
	s_movk_i32 s2, 0x440
	v_mad_u32_u24 v71, v69, s2, v70
	v_lshl_add_u32 v71, v68, 2, v71
	v_lshrrev_b32_e32 v72, 4, v66
	s_movk_i32 s3, 0x110
	v_mad_u32_u24 v78, v72, s3, v70
	v_lshl_add_u32 v78, v68, 4, v78
	v_lshrrev_b32_e32 v73, 1, v67
	v_lshl_add_u32 v79, v73, 6, v72
	v_and_b32_e32 v73, 1, v67
	v_lshlrev_b32_e32 v73, 8, v73
	v_lshl_add_u32 v73, v79, 11, v73
	v_lshl_add_u32 v73, v68, 4, v73
	v_and_b32_e32 v72, 0x4f, v0
	v_lshlrev_b32_e32 v72, 2, v72
	s_waitcnt lgkmcnt(0)
	s_lshl_b32 s2, s25, 2
	s_add_u32 s28, s28, s2
	s_addc_u32 s29, s29, 0
	global_load_dword v74, v72, s[28:29]
	global_load_dword v75, v72, s[28:29] offset:64
	global_load_dword v76, v72, s[28:29] offset:128
	global_load_dword v77, v72, s[28:29] offset:192
	s_lshl_b32 s2, s24, 11
	s_lshl_b32 s3, s25, 2
	s_add_u32 s2, s2, s3
	s_add_u32 s34, s30, s2
	s_addc_u32 s35, s31, 0
	s_add_u32 s36, s32, s2
	s_addc_u32 s37, s33, 0
	s_mov_b64 s[38:39], s[34:35]
	global_load_dwordx4 v[100:103], v73, s[38:39]
	s_add_u32 s38, s34, 0x2000
	s_addc_u32 s39, s35, 0
	global_load_dwordx4 v[104:107], v73, s[38:39]
	s_add_u32 s38, s34, 0x4000
	s_addc_u32 s39, s35, 0
	global_load_dwordx4 v[108:111], v73, s[38:39]
	s_add_u32 s38, s34, 0x6000
	s_addc_u32 s39, s35, 0
	global_load_dwordx4 v[112:115], v73, s[38:39]
	s_add_u32 s38, s34, 0x8000
	s_addc_u32 s39, s35, 0
	global_load_dwordx4 v[116:119], v73, s[38:39]
	s_add_u32 s38, s34, 0xa000
	s_addc_u32 s39, s35, 0
	global_load_dwordx4 v[120:123], v73, s[38:39]
	s_add_u32 s38, s34, 0xc000
	s_addc_u32 s39, s35, 0
	global_load_dwordx4 v[124:127], v73, s[38:39]
	s_add_u32 s38, s34, 0xe000
	s_addc_u32 s39, s35, 0
	global_load_dwordx4 v[128:131], v73, s[38:39]
	s_add_u32 s38, s34, 0x10000
	s_addc_u32 s39, s35, 0
	global_load_dwordx4 v[132:135], v73, s[38:39]
	s_add_u32 s38, s34, 0x12000
	s_addc_u32 s39, s35, 0
	global_load_dwordx4 v[136:139], v73, s[38:39]
	s_add_u32 s38, s34, 0x14000
	s_addc_u32 s39, s35, 0
	global_load_dwordx4 v[140:143], v73, s[38:39]
	s_add_u32 s38, s34, 0x16000
	s_addc_u32 s39, s35, 0
	global_load_dwordx4 v[144:147], v73, s[38:39]
	s_add_u32 s38, s34, 0x18000
	s_addc_u32 s39, s35, 0
	global_load_dwordx4 v[148:151], v73, s[38:39]
	s_add_u32 s38, s34, 0x1a000
	s_addc_u32 s39, s35, 0
	global_load_dwordx4 v[152:155], v73, s[38:39]
	s_add_u32 s38, s34, 0x1c000
	s_addc_u32 s39, s35, 0
	global_load_dwordx4 v[156:159], v73, s[38:39]
	s_add_u32 s38, s34, 0x1e000
	s_addc_u32 s39, s35, 0
	global_load_dwordx4 v[160:163], v73, s[38:39]
	s_waitcnt vmcnt(16)
	v_fmamk_f32 v62, v62, 0x35800000, v74
	v_fmamk_f32 v63, v63, 0x35800000, v74
	v_fmamk_f32 v64, v64, 0x35800000, v74
	v_fmamk_f32 v65, v65, 0x35800000, v74
	v_fmamk_f32 v58, v58, 0x35800000, v75
	v_fmamk_f32 v59, v59, 0x35800000, v75
	v_fmamk_f32 v60, v60, 0x35800000, v75
	v_fmamk_f32 v61, v61, 0x35800000, v75
	v_fmamk_f32 v54, v54, 0x35800000, v76
	v_fmamk_f32 v55, v55, 0x35800000, v76
	v_fmamk_f32 v56, v56, 0x35800000, v76
	v_fmamk_f32 v57, v57, 0x35800000, v76
	v_fmamk_f32 v50, v50, 0x35800000, v77
	v_fmamk_f32 v51, v51, 0x35800000, v77
	v_fmamk_f32 v52, v52, 0x35800000, v77
	v_fmamk_f32 v53, v53, 0x35800000, v77
	ds_write_b32 v71, v62
	ds_write_b32 v71, v63 offset:272
	ds_write_b32 v71, v64 offset:544
	ds_write_b32 v71, v65 offset:816
	ds_write_b32 v71, v58 offset:64
	ds_write_b32 v71, v59 offset:336
	ds_write_b32 v71, v60 offset:608
	ds_write_b32 v71, v61 offset:880
	ds_write_b32 v71, v54 offset:128
	ds_write_b32 v71, v55 offset:400
	ds_write_b32 v71, v56 offset:672
	ds_write_b32 v71, v57 offset:944
	ds_write_b32 v71, v50 offset:192
	ds_write_b32 v71, v51 offset:464
	ds_write_b32 v71, v52 offset:736
	ds_write_b32 v71, v53 offset:1008
	ds_read_b128 v[164:167], v78
	ds_read_b128 v[168:171], v78 offset:1088
	ds_read_b128 v[172:175], v78 offset:2176
	ds_read_b128 v[176:179], v78 offset:3264
	s_waitcnt lgkmcnt(0)
	s_waitcnt vmcnt(15)
	v_add_f32_e32 v164, v100, v164
	v_add_f32_e32 v165, v101, v165
	v_add_f32_e32 v166, v102, v166
	v_add_f32_e32 v167, v103, v167
	s_mov_b64 s[38:39], s[36:37]
	global_store_dwordx4 v73, v[164:167], s[38:39]
	s_waitcnt vmcnt(15)
	v_add_f32_e32 v168, v104, v168
	v_add_f32_e32 v169, v105, v169
	v_add_f32_e32 v170, v106, v170
	v_add_f32_e32 v171, v107, v171
	s_add_u32 s38, s36, 0x2000
	s_addc_u32 s39, s37, 0
	global_store_dwordx4 v73, v[168:171], s[38:39]
	s_waitcnt vmcnt(15)
	v_add_f32_e32 v172, v108, v172
	v_add_f32_e32 v173, v109, v173
	v_add_f32_e32 v174, v110, v174
	v_add_f32_e32 v175, v111, v175
	s_add_u32 s38, s36, 0x4000
	s_addc_u32 s39, s37, 0
	global_store_dwordx4 v73, v[172:175], s[38:39]
	s_waitcnt vmcnt(15)
	v_add_f32_e32 v176, v112, v176
	v_add_f32_e32 v177, v113, v177
	v_add_f32_e32 v178, v114, v178
	v_add_f32_e32 v179, v115, v179
	s_add_u32 s38, s36, 0x6000
	s_addc_u32 s39, s37, 0
	global_store_dwordx4 v73, v[176:179], s[38:39]
	v_fmamk_f32 v46, v46, 0x35800000, v74
	v_fmamk_f32 v47, v47, 0x35800000, v74
	v_fmamk_f32 v48, v48, 0x35800000, v74
	v_fmamk_f32 v49, v49, 0x35800000, v74
	v_fmamk_f32 v42, v42, 0x35800000, v75
	v_fmamk_f32 v43, v43, 0x35800000, v75
	v_fmamk_f32 v44, v44, 0x35800000, v75
	v_fmamk_f32 v45, v45, 0x35800000, v75
	v_fmamk_f32 v38, v38, 0x35800000, v76
	v_fmamk_f32 v39, v39, 0x35800000, v76
	v_fmamk_f32 v40, v40, 0x35800000, v76
	v_fmamk_f32 v41, v41, 0x35800000, v76
	v_fmamk_f32 v34, v34, 0x35800000, v77
	v_fmamk_f32 v35, v35, 0x35800000, v77
	v_fmamk_f32 v36, v36, 0x35800000, v77
	v_fmamk_f32 v37, v37, 0x35800000, v77
	ds_write_b32 v71, v46
	ds_write_b32 v71, v47 offset:272
	ds_write_b32 v71, v48 offset:544
	ds_write_b32 v71, v49 offset:816
	ds_write_b32 v71, v42 offset:64
	ds_write_b32 v71, v43 offset:336
	ds_write_b32 v71, v44 offset:608
	ds_write_b32 v71, v45 offset:880
	ds_write_b32 v71, v38 offset:128
	ds_write_b32 v71, v39 offset:400
	ds_write_b32 v71, v40 offset:672
	ds_write_b32 v71, v41 offset:944
	ds_write_b32 v71, v34 offset:192
	ds_write_b32 v71, v35 offset:464
	ds_write_b32 v71, v36 offset:736
	ds_write_b32 v71, v37 offset:1008
	ds_read_b128 v[180:183], v78
	ds_read_b128 v[184:187], v78 offset:1088
	ds_read_b128 v[188:191], v78 offset:2176
	ds_read_b128 v[192:195], v78 offset:3264
	s_waitcnt lgkmcnt(0)
	s_waitcnt vmcnt(15)
	v_add_f32_e32 v180, v116, v180
	v_add_f32_e32 v181, v117, v181
	v_add_f32_e32 v182, v118, v182
	v_add_f32_e32 v183, v119, v183
	s_add_u32 s38, s36, 0x8000
	s_addc_u32 s39, s37, 0
	global_store_dwordx4 v73, v[180:183], s[38:39]
	s_waitcnt vmcnt(15)
	v_add_f32_e32 v184, v120, v184
	v_add_f32_e32 v185, v121, v185
	v_add_f32_e32 v186, v122, v186
	v_add_f32_e32 v187, v123, v187
	s_add_u32 s38, s36, 0xa000
	s_addc_u32 s39, s37, 0
	global_store_dwordx4 v73, v[184:187], s[38:39]
	s_waitcnt vmcnt(15)
	v_add_f32_e32 v188, v124, v188
	v_add_f32_e32 v189, v125, v189
	v_add_f32_e32 v190, v126, v190
	v_add_f32_e32 v191, v127, v191
	s_add_u32 s38, s36, 0xc000
	s_addc_u32 s39, s37, 0
	global_store_dwordx4 v73, v[188:191], s[38:39]
	s_waitcnt vmcnt(15)
	v_add_f32_e32 v192, v128, v192
	v_add_f32_e32 v193, v129, v193
	v_add_f32_e32 v194, v130, v194
	v_add_f32_e32 v195, v131, v195
	s_add_u32 s38, s36, 0xe000
	s_addc_u32 s39, s37, 0
	global_store_dwordx4 v73, v[192:195], s[38:39]
	v_fmamk_f32 v30, v30, 0x35800000, v74
	v_fmamk_f32 v31, v31, 0x35800000, v74
	v_fmamk_f32 v32, v32, 0x35800000, v74
	v_fmamk_f32 v33, v33, 0x35800000, v74
	v_fmamk_f32 v26, v26, 0x35800000, v75
	v_fmamk_f32 v27, v27, 0x35800000, v75
	v_fmamk_f32 v28, v28, 0x35800000, v75
	v_fmamk_f32 v29, v29, 0x35800000, v75
	v_fmamk_f32 v22, v22, 0x35800000, v76
	v_fmamk_f32 v23, v23, 0x35800000, v76
	v_fmamk_f32 v24, v24, 0x35800000, v76
	v_fmamk_f32 v25, v25, 0x35800000, v76
	v_fmamk_f32 v18, v18, 0x35800000, v77
	v_fmamk_f32 v19, v19, 0x35800000, v77
	v_fmamk_f32 v20, v20, 0x35800000, v77
	v_fmamk_f32 v21, v21, 0x35800000, v77
	ds_write_b32 v71, v30
	ds_write_b32 v71, v31 offset:272
	ds_write_b32 v71, v32 offset:544
	ds_write_b32 v71, v33 offset:816
	ds_write_b32 v71, v26 offset:64
	ds_write_b32 v71, v27 offset:336
	ds_write_b32 v71, v28 offset:608
	ds_write_b32 v71, v29 offset:880
	ds_write_b32 v71, v22 offset:128
	ds_write_b32 v71, v23 offset:400
	ds_write_b32 v71, v24 offset:672
	ds_write_b32 v71, v25 offset:944
	ds_write_b32 v71, v18 offset:192
	ds_write_b32 v71, v19 offset:464
	ds_write_b32 v71, v20 offset:736
	ds_write_b32 v71, v21 offset:1008
	ds_read_b128 v[164:167], v78
	ds_read_b128 v[168:171], v78 offset:1088
	ds_read_b128 v[172:175], v78 offset:2176
	ds_read_b128 v[176:179], v78 offset:3264
	s_waitcnt lgkmcnt(0)
	s_waitcnt vmcnt(15)
	v_add_f32_e32 v164, v132, v164
	v_add_f32_e32 v165, v133, v165
	v_add_f32_e32 v166, v134, v166
	v_add_f32_e32 v167, v135, v167
	s_add_u32 s38, s36, 0x10000
	s_addc_u32 s39, s37, 0
	global_store_dwordx4 v73, v[164:167], s[38:39]
	s_waitcnt vmcnt(15)
	v_add_f32_e32 v168, v136, v168
	v_add_f32_e32 v169, v137, v169
	v_add_f32_e32 v170, v138, v170
	v_add_f32_e32 v171, v139, v171
	s_add_u32 s38, s36, 0x12000
	s_addc_u32 s39, s37, 0
	global_store_dwordx4 v73, v[168:171], s[38:39]
	s_waitcnt vmcnt(15)
	v_add_f32_e32 v172, v140, v172
	v_add_f32_e32 v173, v141, v173
	v_add_f32_e32 v174, v142, v174
	v_add_f32_e32 v175, v143, v175
	s_add_u32 s38, s36, 0x14000
	s_addc_u32 s39, s37, 0
	global_store_dwordx4 v73, v[172:175], s[38:39]
	s_waitcnt vmcnt(15)
	v_add_f32_e32 v176, v144, v176
	v_add_f32_e32 v177, v145, v177
	v_add_f32_e32 v178, v146, v178
	v_add_f32_e32 v179, v147, v179
	s_add_u32 s38, s36, 0x16000
	s_addc_u32 s39, s37, 0
	global_store_dwordx4 v73, v[176:179], s[38:39]
	v_fmamk_f32 v14, v14, 0x35800000, v74
	v_fmamk_f32 v15, v15, 0x35800000, v74
	v_fmamk_f32 v16, v16, 0x35800000, v74
	v_fmamk_f32 v17, v17, 0x35800000, v74
	v_fmamk_f32 v10, v10, 0x35800000, v75
	v_fmamk_f32 v11, v11, 0x35800000, v75
	v_fmamk_f32 v12, v12, 0x35800000, v75
	v_fmamk_f32 v13, v13, 0x35800000, v75
	v_fmamk_f32 v6, v6, 0x35800000, v76
	v_fmamk_f32 v7, v7, 0x35800000, v76
	v_fmamk_f32 v8, v8, 0x35800000, v76
	v_fmamk_f32 v9, v9, 0x35800000, v76
	v_fmamk_f32 v2, v2, 0x35800000, v77
	v_fmamk_f32 v3, v3, 0x35800000, v77
	v_fmamk_f32 v4, v4, 0x35800000, v77
	v_fmamk_f32 v5, v5, 0x35800000, v77
	ds_write_b32 v71, v14
	ds_write_b32 v71, v15 offset:272
	ds_write_b32 v71, v16 offset:544
	ds_write_b32 v71, v17 offset:816
	ds_write_b32 v71, v10 offset:64
	ds_write_b32 v71, v11 offset:336
	ds_write_b32 v71, v12 offset:608
	ds_write_b32 v71, v13 offset:880
	ds_write_b32 v71, v6 offset:128
	ds_write_b32 v71, v7 offset:400
	ds_write_b32 v71, v8 offset:672
	ds_write_b32 v71, v9 offset:944
	ds_write_b32 v71, v2 offset:192
	ds_write_b32 v71, v3 offset:464
	ds_write_b32 v71, v4 offset:736
	ds_write_b32 v71, v5 offset:1008
	ds_read_b128 v[180:183], v78
	ds_read_b128 v[184:187], v78 offset:1088
	ds_read_b128 v[188:191], v78 offset:2176
	ds_read_b128 v[192:195], v78 offset:3264
	s_waitcnt lgkmcnt(0)
	s_waitcnt vmcnt(15)
	v_add_f32_e32 v180, v148, v180
	v_add_f32_e32 v181, v149, v181
	v_add_f32_e32 v182, v150, v182
	v_add_f32_e32 v183, v151, v183
	s_add_u32 s38, s36, 0x18000
	s_addc_u32 s39, s37, 0
	global_store_dwordx4 v73, v[180:183], s[38:39]
	s_waitcnt vmcnt(15)
	v_add_f32_e32 v184, v152, v184
	v_add_f32_e32 v185, v153, v185
	v_add_f32_e32 v186, v154, v186
	v_add_f32_e32 v187, v155, v187
	s_add_u32 s38, s36, 0x1a000
	s_addc_u32 s39, s37, 0
	global_store_dwordx4 v73, v[184:187], s[38:39]
	s_waitcnt vmcnt(15)
	v_add_f32_e32 v188, v156, v188
	v_add_f32_e32 v189, v157, v189
	v_add_f32_e32 v190, v158, v190
	v_add_f32_e32 v191, v159, v191
	s_add_u32 s38, s36, 0x1c000
	s_addc_u32 s39, s37, 0
	global_store_dwordx4 v73, v[188:191], s[38:39]
	s_waitcnt vmcnt(15)
	v_add_f32_e32 v192, v160, v192
	v_add_f32_e32 v193, v161, v193
	v_add_f32_e32 v194, v162, v194
	v_add_f32_e32 v195, v163, v195
	s_add_u32 s38, s36, 0x1e000
	s_addc_u32 s39, s37, 0
	global_store_dwordx4 v73, v[192:195], s[38:39]
	s_endpgm
	.p2alignl 8, 3212836864

.LBB12_47:
	s_mov_b32 s60, s23
	s_mov_b32 s61, s27
	s_mov_b32 s62, s25
	s_mov_b32 s63, s26
	s_mov_b32 s64, s22
	s_mov_b32 s24, s60
	s_mov_b32 s25, s61
	s_mov_b32 s26, s62
	s_mov_b32 s27, s63
	s_mov_b32 s46, s64
	s_load_dwordx2 s[28:29], s[0:1], 0x58
	s_load_dwordx2 s[30:31], s[0:1], 0x70
	s_load_dwordx2 s[40:41], s[0:1], 0x78
	s_load_dwordx2 s[42:43], s[0:1], 0x80
	s_load_dwordx2 s[44:45], s[0:1], 0x60
	v_and_b32_e32 v66, 63, v0
	v_lshrrev_b32_e32 v67, 6, v0
	v_and_b32_e32 v68, 15, v0
	v_bfe_u32 v69, v0, 4, 2
	v_mul_u32_u24_e32 v70, 0x2000, v67
	s_movk_i32 s2, 0x440
	v_mad_u32_u24 v71, v69, s2, v70
	v_lshl_add_u32 v71, v68, 2, v71
	v_lshrrev_b32_e32 v72, 4, v66
	s_movk_i32 s3, 0x110
	v_mad_u32_u24 v78, v72, s3, v70
	v_lshl_add_u32 v78, v68, 4, v78
	v_lshrrev_b32_e32 v73, 1, v67
	v_lshl_add_u32 v79, v73, 6, v72
	v_and_b32_e32 v73, 1, v67
	v_lshlrev_b32_e32 v73, 8, v73
	v_lshl_add_u32 v73, v79, 11, v73
	v_lshl_add_u32 v73, v68, 4, v73
	v_and_b32_e32 v72, 0x4f, v0
	v_lshlrev_b32_e32 v72, 2, v72
	s_waitcnt lgkmcnt(0)
	s_mul_i32 s2, s26, s44
	s_add_i32 s2, s2, s25
	s_lshl_b32 s2, s2, 2
	s_add_u32 s28, s28, s2
	s_addc_u32 s29, s29, 0
	global_load_dword v74, v72, s[28:29]
	global_load_dword v75, v72, s[28:29] offset:64
	global_load_dword v76, v72, s[28:29] offset:128
	global_load_dword v77, v72, s[28:29] offset:192
	s_lshl_b32 s2, s24, 11
	s_lshl_b32 s3, s25, 2
	s_add_u32 s2, s2, s3
	s_cmp_eq_u32 s46, 1
	s_cselect_b32 s40, s42, s40
	s_cselect_b32 s41, s43, s41
	s_add_u32 s36, s40, s2
	s_addc_u32 s37, s41, 0
	v_lshrrev_b32_e32 v80, 7, v0
	v_lshlrev_b32_e32 v80, 6, v80
	v_lshl_add_u32 v80, v69, 2, v80
	s_lshl_b32 s2, s24, 2
	s_add_u32 s30, s30, s2
	s_addc_u32 s31, s31, 0
	v_lshlrev_b32_e32 v81, 2, v80
	global_load_dword v84, v81, s[30:31]
	global_load_dword v85, v81, s[30:31] offset:4
	global_load_dword v86, v81, s[30:31] offset:8
	global_load_dword v87, v81, s[30:31] offset:12
	global_load_dword v88, v81, s[30:31] offset:64
	global_load_dword v89, v81, s[30:31] offset:68
	global_load_dword v90, v81, s[30:31] offset:72
	global_load_dword v91, v81, s[30:31] offset:76
	global_load_dword v92, v81, s[30:31] offset:128
	global_load_dword v93, v81, s[30:31] offset:132
	global_load_dword v94, v81, s[30:31] offset:136
	global_load_dword v95, v81, s[30:31] offset:140
	global_load_dword v96, v81, s[30:31] offset:192
	global_load_dword v97, v81, s[30:31] offset:196
	global_load_dword v98, v81, s[30:31] offset:200
	global_load_dword v99, v81, s[30:31] offset:204
	s_sub_i32 s47, s27, s24
	s_cmp_eq_u32 s46, 1
	s_cselect_b32 s2, 0, 1.0
	s_waitcnt vmcnt(16)
	v_mul_f32_e32 v74, s2, v74
	v_mul_f32_e32 v75, s2, v75
	v_mul_f32_e32 v76, s2, v76
	v_mul_f32_e32 v77, s2, v77
	s_waitcnt vmcnt(0)
	v_add_u32_e32 v82, 0, v80
	v_cmp_gt_i32_e32 vcc, s47, v82
	s_nop 1
	v_cndmask_b32_e32 v84, 0, v84, vcc
	v_add_u32_e32 v82, 1, v80
	v_cmp_gt_i32_e32 vcc, s47, v82
	s_nop 1
	v_cndmask_b32_e32 v85, 0, v85, vcc
	v_add_u32_e32 v82, 2, v80
	v_cmp_gt_i32_e32 vcc, s47, v82
	s_nop 1
	v_cndmask_b32_e32 v86, 0, v86, vcc
	v_add_u32_e32 v82, 3, v80
	v_cmp_gt_i32_e32 vcc, s47, v82
	s_nop 1
	v_cndmask_b32_e32 v87, 0, v87, vcc
	v_add_u32_e32 v82, 16, v80
	v_cmp_gt_i32_e32 vcc, s47, v82
	s_nop 1
	v_cndmask_b32_e32 v88, 0, v88, vcc
	v_add_u32_e32 v82, 17, v80
	v_cmp_gt_i32_e32 vcc, s47, v82
	s_nop 1
	v_cndmask_b32_e32 v89, 0, v89, vcc
	v_add_u32_e32 v82, 18, v80
	v_cmp_gt_i32_e32 vcc, s47, v82
	s_nop 1
	v_cndmask_b32_e32 v90, 0, v90, vcc
	v_add_u32_e32 v82, 19, v80
	v_cmp_gt_i32_e32 vcc, s47, v82
	s_nop 1
	v_cndmask_b32_e32 v91, 0, v91, vcc
	v_add_u32_e32 v82, 32, v80
	v_cmp_gt_i32_e32 vcc, s47, v82
	s_nop 1
	v_cndmask_b32_e32 v92, 0, v92, vcc
	v_add_u32_e32 v82, 33, v80
	v_cmp_gt_i32_e32 vcc, s47, v82
	s_nop 1
	v_cndmask_b32_e32 v93, 0, v93, vcc
	v_add_u32_e32 v82, 34, v80
	v_cmp_gt_i32_e32 vcc, s47, v82
	s_nop 1
	v_cndmask_b32_e32 v94, 0, v94, vcc
	v_add_u32_e32 v82, 35, v80
	v_cmp_gt_i32_e32 vcc, s47, v82
	s_nop 1
	v_cndmask_b32_e32 v95, 0, v95, vcc
	v_add_u32_e32 v82, 48, v80
	v_cmp_gt_i32_e32 vcc, s47, v82
	s_nop 1
	v_cndmask_b32_e32 v96, 0, v96, vcc
	v_add_u32_e32 v82, 49, v80
	v_cmp_gt_i32_e32 vcc, s47, v82
	s_nop 1
	v_cndmask_b32_e32 v97, 0, v97, vcc
	v_add_u32_e32 v82, 50, v80
	v_cmp_gt_i32_e32 vcc, s47, v82
	s_nop 1
	v_cndmask_b32_e32 v98, 0, v98, vcc
	v_add_u32_e32 v82, 51, v80
	v_cmp_gt_i32_e32 vcc, s47, v82
	s_nop 1
	v_cndmask_b32_e32 v99, 0, v99, vcc
	v_fmamk_f32 v62, v62, 0x35800000, v74
	v_fmamk_f32 v63, v63, 0x35800000, v74
	v_fmamk_f32 v64, v64, 0x35800000, v74
	v_fmamk_f32 v65, v65, 0x35800000, v74
	v_fmamk_f32 v58, v58, 0x35800000, v75
	v_fmamk_f32 v59, v59, 0x35800000, v75
	v_fmamk_f32 v60, v60, 0x35800000, v75
	v_fmamk_f32 v61, v61, 0x35800000, v75
	v_fmamk_f32 v54, v54, 0x35800000, v76
	v_fmamk_f32 v55, v55, 0x35800000, v76
	v_fmamk_f32 v56, v56, 0x35800000, v76
	v_fmamk_f32 v57, v57, 0x35800000, v76
	v_fmamk_f32 v50, v50, 0x35800000, v77
	v_fmamk_f32 v51, v51, 0x35800000, v77
	v_fmamk_f32 v52, v52, 0x35800000, v77
	v_fmamk_f32 v53, v53, 0x35800000, v77
	v_mul_f32_e32 v62, v62, v84
	v_mul_f32_e32 v63, v63, v85
	v_mul_f32_e32 v64, v64, v86
	v_mul_f32_e32 v65, v65, v87
	v_mul_f32_e32 v58, v58, v84
	v_mul_f32_e32 v59, v59, v85
	v_mul_f32_e32 v60, v60, v86
	v_mul_f32_e32 v61, v61, v87
	v_mul_f32_e32 v54, v54, v84
	v_mul_f32_e32 v55, v55, v85
	v_mul_f32_e32 v56, v56, v86
	v_mul_f32_e32 v57, v57, v87
	v_mul_f32_e32 v50, v50, v84
	v_mul_f32_e32 v51, v51, v85
	v_mul_f32_e32 v52, v52, v86
	v_mul_f32_e32 v53, v53, v87
	ds_write_b32 v71, v62
	ds_write_b32 v71, v63 offset:272
	ds_write_b32 v71, v64 offset:544
	ds_write_b32 v71, v65 offset:816
	ds_write_b32 v71, v58 offset:64
	ds_write_b32 v71, v59 offset:336
	ds_write_b32 v71, v60 offset:608
	ds_write_b32 v71, v61 offset:880
	ds_write_b32 v71, v54 offset:128
	ds_write_b32 v71, v55 offset:400
	ds_write_b32 v71, v56 offset:672
	ds_write_b32 v71, v57 offset:944
	ds_write_b32 v71, v50 offset:192
	ds_write_b32 v71, v51 offset:464
	ds_write_b32 v71, v52 offset:736
	ds_write_b32 v71, v53 offset:1008
	ds_read_b128 v[100:103], v78
	ds_read_b128 v[104:107], v78 offset:1088
	ds_read_b128 v[108:111], v78 offset:2176
	ds_read_b128 v[112:115], v78 offset:3264
	s_waitcnt lgkmcnt(0)
	s_mov_b64 s[38:39], s[36:37]
	s_sub_i32 s2, s47, 0
	v_cmp_gt_i32_e32 vcc, s2, v79
	s_and_saveexec_b64 s[48:49], vcc
	global_store_dwordx4 v73, v[100:103], s[38:39]
	s_mov_b64 exec, s[48:49]
	s_add_u32 s38, s36, 0x2000
	s_addc_u32 s39, s37, 0
	s_sub_i32 s2, s47, 4
	v_cmp_gt_i32_e32 vcc, s2, v79
	s_and_saveexec_b64 s[48:49], vcc
	global_store_dwordx4 v73, v[104:107], s[38:39]
	s_mov_b64 exec, s[48:49]
	s_add_u32 s38, s36, 0x4000
	s_addc_u32 s39, s37, 0
	s_sub_i32 s2, s47, 8
	v_cmp_gt_i32_e32 vcc, s2, v79
	s_and_saveexec_b64 s[48:49], vcc
	global_store_dwordx4 v73, v[108:111], s[38:39]
	s_mov_b64 exec, s[48:49]
	s_add_u32 s38, s36, 0x6000
	s_addc_u32 s39, s37, 0
	s_sub_i32 s2, s47, 12
	v_cmp_gt_i32_e32 vcc, s2, v79
	s_and_saveexec_b64 s[48:49], vcc
	global_store_dwordx4 v73, v[112:115], s[38:39]
	s_mov_b64 exec, s[48:49]
	v_fmamk_f32 v46, v46, 0x35800000, v74
	v_fmamk_f32 v47, v47, 0x35800000, v74
	v_fmamk_f32 v48, v48, 0x35800000, v74
	v_fmamk_f32 v49, v49, 0x35800000, v74
	v_fmamk_f32 v42, v42, 0x35800000, v75
	v_fmamk_f32 v43, v43, 0x35800000, v75
	v_fmamk_f32 v44, v44, 0x35800000, v75
	v_fmamk_f32 v45, v45, 0x35800000, v75
	v_fmamk_f32 v38, v38, 0x35800000, v76
	v_fmamk_f32 v39, v39, 0x35800000, v76
	v_fmamk_f32 v40, v40, 0x35800000, v76
	v_fmamk_f32 v41, v41, 0x35800000, v76
	v_fmamk_f32 v34, v34, 0x35800000, v77
	v_fmamk_f32 v35, v35, 0x35800000, v77
	v_fmamk_f32 v36, v36, 0x35800000, v77
	v_fmamk_f32 v37, v37, 0x35800000, v77
	v_mul_f32_e32 v46, v46, v88
	v_mul_f32_e32 v47, v47, v89
	v_mul_f32_e32 v48, v48, v90
	v_mul_f32_e32 v49, v49, v91
	v_mul_f32_e32 v42, v42, v88
	v_mul_f32_e32 v43, v43, v89
	v_mul_f32_e32 v44, v44, v90
	v_mul_f32_e32 v45, v45, v91
	v_mul_f32_e32 v38, v38, v88
	v_mul_f32_e32 v39, v39, v89
	v_mul_f32_e32 v40, v40, v90
	v_mul_f32_e32 v41, v41, v91
	v_mul_f32_e32 v34, v34, v88
	v_mul_f32_e32 v35, v35, v89
	v_mul_f32_e32 v36, v36, v90
	v_mul_f32_e32 v37, v37, v91
	ds_write_b32 v71, v46
	ds_write_b32 v71, v47 offset:272
	ds_write_b32 v71, v48 offset:544
	ds_write_b32 v71, v49 offset:816
	ds_write_b32 v71, v42 offset:64
	ds_write_b32 v71, v43 offset:336
	ds_write_b32 v71, v44 offset:608
	ds_write_b32 v71, v45 offset:880
	ds_write_b32 v71, v38 offset:128
	ds_write_b32 v71, v39 offset:400
	ds_write_b32 v71, v40 offset:672
	ds_write_b32 v71, v41 offset:944
	ds_write_b32 v71, v34 offset:192
	ds_write_b32 v71, v35 offset:464
	ds_write_b32 v71, v36 offset:736
	ds_write_b32 v71, v37 offset:1008
	ds_read_b128 v[116:119], v78
	ds_read_b128 v[120:123], v78 offset:1088
	ds_read_b128 v[124:127], v78 offset:2176
	ds_read_b128 v[128:131], v78 offset:3264
	s_waitcnt lgkmcnt(0)
	s_add_u32 s38, s36, 0x8000
	s_addc_u32 s39, s37, 0
	s_sub_i32 s2, s47, 16
	v_cmp_gt_i32_e32 vcc, s2, v79
	s_and_saveexec_b64 s[48:49], vcc
	global_store_dwordx4 v73, v[116:119], s[38:39]
	s_mov_b64 exec, s[48:49]
	s_add_u32 s38, s36, 0xa000
	s_addc_u32 s39, s37, 0
	s_sub_i32 s2, s47, 20
	v_cmp_gt_i32_e32 vcc, s2, v79
	s_and_saveexec_b64 s[48:49], vcc
	global_store_dwordx4 v73, v[120:123], s[38:39]
	s_mov_b64 exec, s[48:49]
	s_add_u32 s38, s36, 0xc000
	s_addc_u32 s39, s37, 0
	s_sub_i32 s2, s47, 24
	v_cmp_gt_i32_e32 vcc, s2, v79
	s_and_saveexec_b64 s[48:49], vcc
	global_store_dwordx4 v73, v[124:127], s[38:39]
	s_mov_b64 exec, s[48:49]
	s_add_u32 s38, s36, 0xe000
	s_addc_u32 s39, s37, 0
	s_sub_i32 s2, s47, 28
	v_cmp_gt_i32_e32 vcc, s2, v79
	s_and_saveexec_b64 s[48:49], vcc
	global_store_dwordx4 v73, v[128:131], s[38:39]
	s_mov_b64 exec, s[48:49]
	v_fmamk_f32 v30, v30, 0x35800000, v74
	v_fmamk_f32 v31, v31, 0x35800000, v74
	v_fmamk_f32 v32, v32, 0x35800000, v74
	v_fmamk_f32 v33, v33, 0x35800000, v74
	v_fmamk_f32 v26, v26, 0x35800000, v75
	v_fmamk_f32 v27, v27, 0x35800000, v75
	v_fmamk_f32 v28, v28, 0x35800000, v75
	v_fmamk_f32 v29, v29, 0x35800000, v75
	v_fmamk_f32 v22, v22, 0x35800000, v76
	v_fmamk_f32 v23, v23, 0x35800000, v76
	v_fmamk_f32 v24, v24, 0x35800000, v76
	v_fmamk_f32 v25, v25, 0x35800000, v76
	v_fmamk_f32 v18, v18, 0x35800000, v77
	v_fmamk_f32 v19, v19, 0x35800000, v77
	v_fmamk_f32 v20, v20, 0x35800000, v77
	v_fmamk_f32 v21, v21, 0x35800000, v77
	v_mul_f32_e32 v30, v30, v92
	v_mul_f32_e32 v31, v31, v93
	v_mul_f32_e32 v32, v32, v94
	v_mul_f32_e32 v33, v33, v95
	v_mul_f32_e32 v26, v26, v92
	v_mul_f32_e32 v27, v27, v93
	v_mul_f32_e32 v28, v28, v94
	v_mul_f32_e32 v29, v29, v95
	v_mul_f32_e32 v22, v22, v92
	v_mul_f32_e32 v23, v23, v93
	v_mul_f32_e32 v24, v24, v94
	v_mul_f32_e32 v25, v25, v95
	v_mul_f32_e32 v18, v18, v92
	v_mul_f32_e32 v19, v19, v93
	v_mul_f32_e32 v20, v20, v94
	v_mul_f32_e32 v21, v21, v95
	ds_write_b32 v71, v30
	ds_write_b32 v71, v31 offset:272
	ds_write_b32 v71, v32 offset:544
	ds_write_b32 v71, v33 offset:816
	ds_write_b32 v71, v26 offset:64
	ds_write_b32 v71, v27 offset:336
	ds_write_b32 v71, v28 offset:608
	ds_write_b32 v71, v29 offset:880
	ds_write_b32 v71, v22 offset:128
	ds_write_b32 v71, v23 offset:400
	ds_write_b32 v71, v24 offset:672
	ds_write_b32 v71, v25 offset:944
	ds_write_b32 v71, v18 offset:192
	ds_write_b32 v71, v19 offset:464
	ds_write_b32 v71, v20 offset:736
	ds_write_b32 v71, v21 offset:1008
	ds_read_b128 v[100:103], v78
	ds_read_b128 v[104:107], v78 offset:1088
	ds_read_b128 v[108:111], v78 offset:2176
	ds_read_b128 v[112:115], v78 offset:3264
	s_waitcnt lgkmcnt(0)
	s_add_u32 s38, s36, 0x10000
	s_addc_u32 s39, s37, 0
	s_sub_i32 s2, s47, 32
	v_cmp_gt_i32_e32 vcc, s2, v79
	s_and_saveexec_b64 s[48:49], vcc
	global_store_dwordx4 v73, v[100:103], s[38:39]
	s_mov_b64 exec, s[48:49]
	s_add_u32 s38, s36, 0x12000
	s_addc_u32 s39, s37, 0
	s_sub_i32 s2, s47, 36
	v_cmp_gt_i32_e32 vcc, s2, v79
	s_and_saveexec_b64 s[48:49], vcc
	global_store_dwordx4 v73, v[104:107], s[38:39]
	s_mov_b64 exec, s[48:49]
	s_add_u32 s38, s36, 0x14000
	s_addc_u32 s39, s37, 0
	s_sub_i32 s2, s47, 40
	v_cmp_gt_i32_e32 vcc, s2, v79
	s_and_saveexec_b64 s[48:49], vcc
	global_store_dwordx4 v73, v[108:111], s[38:39]
	s_mov_b64 exec, s[48:49]
	s_add_u32 s38, s36, 0x16000
	s_addc_u32 s39, s37, 0
	s_sub_i32 s2, s47, 44
	v_cmp_gt_i32_e32 vcc, s2, v79
	s_and_saveexec_b64 s[48:49], vcc
	global_store_dwordx4 v73, v[112:115], s[38:39]
	s_mov_b64 exec, s[48:49]
	v_fmamk_f32 v14, v14, 0x35800000, v74
	v_fmamk_f32 v15, v15, 0x35800000, v74
	v_fmamk_f32 v16, v16, 0x35800000, v74
	v_fmamk_f32 v17, v17, 0x35800000, v74
	v_fmamk_f32 v10, v10, 0x35800000, v75
	v_fmamk_f32 v11, v11, 0x35800000, v75
	v_fmamk_f32 v12, v12, 0x35800000, v75
	v_fmamk_f32 v13, v13, 0x35800000, v75
	v_fmamk_f32 v6, v6, 0x35800000, v76
	v_fmamk_f32 v7, v7, 0x35800000, v76
	v_fmamk_f32 v8, v8, 0x35800000, v76
	v_fmamk_f32 v9, v9, 0x35800000, v76
	v_fmamk_f32 v2, v2, 0x35800000, v77
	v_fmamk_f32 v3, v3, 0x35800000, v77
	v_fmamk_f32 v4, v4, 0x35800000, v77
	v_fmamk_f32 v5, v5, 0x35800000, v77
	v_mul_f32_e32 v14, v14, v96
	v_mul_f32_e32 v15, v15, v97
	v_mul_f32_e32 v16, v16, v98
	v_mul_f32_e32 v17, v17, v99
	v_mul_f32_e32 v10, v10, v96
	v_mul_f32_e32 v11, v11, v97
	v_mul_f32_e32 v12, v12, v98
	v_mul_f32_e32 v13, v13, v99
	v_mul_f32_e32 v6, v6, v96
	v_mul_f32_e32 v7, v7, v97
	v_mul_f32_e32 v8, v8, v98
	v_mul_f32_e32 v9, v9, v99
	v_mul_f32_e32 v2, v2, v96
	v_mul_f32_e32 v3, v3, v97
	v_mul_f32_e32 v4, v4, v98
	v_mul_f32_e32 v5, v5, v99
	ds_write_b32 v71, v14
	ds_write_b32 v71, v15 offset:272
	ds_write_b32 v71, v16 offset:544
	ds_write_b32 v71, v17 offset:816
	ds_write_b32 v71, v10 offset:64
	ds_write_b32 v71, v11 offset:336
	ds_write_b32 v71, v12 offset:608
	ds_write_b32 v71, v13 offset:880
	ds_write_b32 v71, v6 offset:128
	ds_write_b32 v71, v7 offset:400
	ds_write_b32 v71, v8 offset:672
	ds_write_b32 v71, v9 offset:944
	ds_write_b32 v71, v2 offset:192
	ds_write_b32 v71, v3 offset:464
	ds_write_b32 v71, v4 offset:736
	ds_write_b32 v71, v5 offset:1008
	ds_read_b128 v[116:119], v78
	ds_read_b128 v[120:123], v78 offset:1088
	ds_read_b128 v[124:127], v78 offset:2176
	ds_read_b128 v[128:131], v78 offset:3264
	s_waitcnt lgkmcnt(0)
	s_add_u32 s38, s36, 0x18000
	s_addc_u32 s39, s37, 0
	s_sub_i32 s2, s47, 48
	v_cmp_gt_i32_e32 vcc, s2, v79
	s_and_saveexec_b64 s[48:49], vcc
	global_store_dwordx4 v73, v[116:119], s[38:39]
	s_mov_b64 exec, s[48:49]
	s_add_u32 s38, s36, 0x1a000
	s_addc_u32 s39, s37, 0
	s_sub_i32 s2, s47, 52
	v_cmp_gt_i32_e32 vcc, s2, v79
	s_and_saveexec_b64 s[48:49], vcc
	global_store_dwordx4 v73, v[120:123], s[38:39]
	s_mov_b64 exec, s[48:49]
	s_add_u32 s38, s36, 0x1c000
	s_addc_u32 s39, s37, 0
	s_sub_i32 s2, s47, 56
	v_cmp_gt_i32_e32 vcc, s2, v79
	s_and_saveexec_b64 s[48:49], vcc
	global_store_dwordx4 v73, v[124:127], s[38:39]
	s_mov_b64 exec, s[48:49]
	s_add_u32 s38, s36, 0x1e000
	s_addc_u32 s39, s37, 0
	s_sub_i32 s2, s47, 60
	v_cmp_gt_i32_e32 vcc, s2, v79
	s_and_saveexec_b64 s[48:49], vcc
	global_store_dwordx4 v73, v[128:131], s[38:39]
	s_mov_b64 exec, s[48:49]
	s_endpgm

.LBB13_47:
	s_mov_b32 s60, s14
	s_mov_b32 s61, s18
	s_mov_b32 s62, s16
	s_mov_b32 s63, s17
	s_mov_b32 s64, s19
	s_mov_b32 s24, s60
	s_mov_b32 s25, s61
	s_mov_b32 s26, s62
	s_mov_b32 s27, s63
	s_mov_b32 s46, s64
	s_load_dwordx2 s[28:29], s[0:1], 0x58
	s_load_dwordx2 s[30:31], s[0:1], 0x70
	s_load_dwordx2 s[40:41], s[0:1], 0x78
	s_load_dwordx2 s[42:43], s[0:1], 0x80
	s_load_dwordx2 s[44:45], s[0:1], 0x60
	v_and_b32_e32 v66, 63, v0
	v_lshrrev_b32_e32 v67, 6, v0
	v_and_b32_e32 v68, 15, v0
	v_bfe_u32 v69, v0, 4, 2
	v_mul_u32_u24_e32 v70, 0x2000, v67
	s_movk_i32 s2, 0x440
	v_mad_u32_u24 v71, v69, s2, v70
	v_lshl_add_u32 v71, v68, 2, v71
	v_lshrrev_b32_e32 v72, 4, v66
	s_movk_i32 s3, 0x110
	v_mad_u32_u24 v78, v72, s3, v70
	v_lshl_add_u32 v78, v68, 4, v78
	v_lshrrev_b32_e32 v73, 1, v67
	v_lshl_add_u32 v79, v73, 6, v72
	v_and_b32_e32 v73, 1, v67
	v_lshlrev_b32_e32 v73, 8, v73
	v_lshl_add_u32 v73, v79, 11, v73
	v_lshl_add_u32 v73, v68, 4, v73
	v_and_b32_e32 v72, 0x4f, v0
	v_lshlrev_b32_e32 v72, 2, v72
	s_waitcnt lgkmcnt(0)
	s_mul_i32 s2, s26, s44
	s_add_i32 s2, s2, s25
	s_lshl_b32 s2, s2, 2
	s_add_u32 s28, s28, s2
	s_addc_u32 s29, s29, 0
	global_load_dword v74, v72, s[28:29]
	global_load_dword v75, v72, s[28:29] offset:64
	global_load_dword v76, v72, s[28:29] offset:128
	global_load_dword v77, v72, s[28:29] offset:192
	s_lshl_b32 s2, s24, 11
	s_lshl_b32 s3, s25, 2
	s_add_u32 s2, s2, s3
	s_cmp_eq_u32 s46, 1
	s_cselect_b32 s40, s42, s40
	s_cselect_b32 s41, s43, s41
	s_add_u32 s36, s40, s2
	s_addc_u32 s37, s41, 0
	v_lshrrev_b32_e32 v80, 7, v0
	v_lshlrev_b32_e32 v80, 6, v80
	v_lshl_add_u32 v80, v69, 2, v80
	s_lshl_b32 s2, s24, 2
	s_add_u32 s30, s30, s2
	s_addc_u32 s31, s31, 0
	v_lshlrev_b32_e32 v81, 2, v80
	global_load_dword v84, v81, s[30:31]
	global_load_dword v85, v81, s[30:31] offset:4
	global_load_dword v86, v81, s[30:31] offset:8
	global_load_dword v87, v81, s[30:31] offset:12
	global_load_dword v88, v81, s[30:31] offset:64
	global_load_dword v89, v81, s[30:31] offset:68
	global_load_dword v90, v81, s[30:31] offset:72
	global_load_dword v91, v81, s[30:31] offset:76
	global_load_dword v92, v81, s[30:31] offset:128
	global_load_dword v93, v81, s[30:31] offset:132
	global_load_dword v94, v81, s[30:31] offset:136
	global_load_dword v95, v81, s[30:31] offset:140
	global_load_dword v96, v81, s[30:31] offset:192
	global_load_dword v97, v81, s[30:31] offset:196
	global_load_dword v98, v81, s[30:31] offset:200
	global_load_dword v99, v81, s[30:31] offset:204
	s_sub_i32 s47, s27, s24
	s_cmp_eq_u32 s46, 1
	s_cselect_b32 s2, 0, 1.0
	s_waitcnt vmcnt(16)
	v_mul_f32_e32 v74, s2, v74
	v_mul_f32_e32 v75, s2, v75
	v_mul_f32_e32 v76, s2, v76
	v_mul_f32_e32 v77, s2, v77
	s_waitcnt vmcnt(0)
	v_add_u32_e32 v82, 0, v80
	v_cmp_gt_i32_e32 vcc, s47, v82
	s_nop 1
	v_cndmask_b32_e32 v84, 0, v84, vcc
	v_add_u32_e32 v82, 1, v80
	v_cmp_gt_i32_e32 vcc, s47, v82
	s_nop 1
	v_cndmask_b32_e32 v85, 0, v85, vcc
	v_add_u32_e32 v82, 2, v80
	v_cmp_gt_i32_e32 vcc, s47, v82
	s_nop 1
	v_cndmask_b32_e32 v86, 0, v86, vcc
	v_add_u32_e32 v82, 3, v80
	v_cmp_gt_i32_e32 vcc, s47, v82
	s_nop 1
	v_cndmask_b32_e32 v87, 0, v87, vcc
	v_add_u32_e32 v82, 16, v80
	v_cmp_gt_i32_e32 vcc, s47, v82
	s_nop 1
	v_cndmask_b32_e32 v88, 0, v88, vcc
	v_add_u32_e32 v82, 17, v80
	v_cmp_gt_i32_e32 vcc, s47, v82
	s_nop 1
	v_cndmask_b32_e32 v89, 0, v89, vcc
	v_add_u32_e32 v82, 18, v80
	v_cmp_gt_i32_e32 vcc, s47, v82
	s_nop 1
	v_cndmask_b32_e32 v90, 0, v90, vcc
	v_add_u32_e32 v82, 19, v80
	v_cmp_gt_i32_e32 vcc, s47, v82
	s_nop 1
	v_cndmask_b32_e32 v91, 0, v91, vcc
	v_add_u32_e32 v82, 32, v80
	v_cmp_gt_i32_e32 vcc, s47, v82
	s_nop 1
	v_cndmask_b32_e32 v92, 0, v92, vcc
	v_add_u32_e32 v82, 33, v80
	v_cmp_gt_i32_e32 vcc, s47, v82
	s_nop 1
	v_cndmask_b32_e32 v93, 0, v93, vcc
	v_add_u32_e32 v82, 34, v80
	v_cmp_gt_i32_e32 vcc, s47, v82
	s_nop 1
	v_cndmask_b32_e32 v94, 0, v94, vcc
	v_add_u32_e32 v82, 35, v80
	v_cmp_gt_i32_e32 vcc, s47, v82
	s_nop 1
	v_cndmask_b32_e32 v95, 0, v95, vcc
	v_add_u32_e32 v82, 48, v80
	v_cmp_gt_i32_e32 vcc, s47, v82
	s_nop 1
	v_cndmask_b32_e32 v96, 0, v96, vcc
	v_add_u32_e32 v82, 49, v80
	v_cmp_gt_i32_e32 vcc, s47, v82
	s_nop 1
	v_cndmask_b32_e32 v97, 0, v97, vcc
	v_add_u32_e32 v82, 50, v80
	v_cmp_gt_i32_e32 vcc, s47, v82
	s_nop 1
	v_cndmask_b32_e32 v98, 0, v98, vcc
	v_add_u32_e32 v82, 51, v80
	v_cmp_gt_i32_e32 vcc, s47, v82
	s_nop 1
	v_cndmask_b32_e32 v99, 0, v99, vcc
	v_fmamk_f32 v62, v62, 0x35800000, v74
	v_fmamk_f32 v63, v63, 0x35800000, v74
	v_fmamk_f32 v64, v64, 0x35800000, v74
	v_fmamk_f32 v65, v65, 0x35800000, v74
	v_fmamk_f32 v58, v58, 0x35800000, v75
	v_fmamk_f32 v59, v59, 0x35800000, v75
	v_fmamk_f32 v60, v60, 0x35800000, v75
	v_fmamk_f32 v61, v61, 0x35800000, v75
	v_fmamk_f32 v54, v54, 0x35800000, v76
	v_fmamk_f32 v55, v55, 0x35800000, v76
	v_fmamk_f32 v56, v56, 0x35800000, v76
	v_fmamk_f32 v57, v57, 0x35800000, v76
	v_fmamk_f32 v50, v50, 0x35800000, v77
	v_fmamk_f32 v51, v51, 0x35800000, v77
	v_fmamk_f32 v52, v52, 0x35800000, v77
	v_fmamk_f32 v53, v53, 0x35800000, v77
	v_mul_f32_e32 v62, v62, v84
	v_mul_f32_e32 v63, v63, v85
	v_mul_f32_e32 v64, v64, v86
	v_mul_f32_e32 v65, v65, v87
	v_mul_f32_e32 v58, v58, v84
	v_mul_f32_e32 v59, v59, v85
	v_mul_f32_e32 v60, v60, v86
	v_mul_f32_e32 v61, v61, v87
	v_mul_f32_e32 v54, v54, v84
	v_mul_f32_e32 v55, v55, v85
	v_mul_f32_e32 v56, v56, v86
	v_mul_f32_e32 v57, v57, v87
	v_mul_f32_e32 v50, v50, v84
	v_mul_f32_e32 v51, v51, v85
	v_mul_f32_e32 v52, v52, v86
	v_mul_f32_e32 v53, v53, v87
	ds_write_b32 v71, v62
	ds_write_b32 v71, v63 offset:272
	ds_write_b32 v71, v64 offset:544
	ds_write_b32 v71, v65 offset:816
	ds_write_b32 v71, v58 offset:64
	ds_write_b32 v71, v59 offset:336
	ds_write_b32 v71, v60 offset:608
	ds_write_b32 v71, v61 offset:880
	ds_write_b32 v71, v54 offset:128
	ds_write_b32 v71, v55 offset:400
	ds_write_b32 v71, v56 offset:672
	ds_write_b32 v71, v57 offset:944
	ds_write_b32 v71, v50 offset:192
	ds_write_b32 v71, v51 offset:464
	ds_write_b32 v71, v52 offset:736
	ds_write_b32 v71, v53 offset:1008
	ds_read_b128 v[100:103], v78
	ds_read_b128 v[104:107], v78 offset:1088
	ds_read_b128 v[108:111], v78 offset:2176
	ds_read_b128 v[112:115], v78 offset:3264
	s_waitcnt lgkmcnt(0)
	s_mov_b64 s[38:39], s[36:37]
	s_sub_i32 s2, s47, 0
	v_cmp_gt_i32_e32 vcc, s2, v79
	s_and_saveexec_b64 s[48:49], vcc
	global_store_dwordx4 v73, v[100:103], s[38:39]
	s_mov_b64 exec, s[48:49]
	s_add_u32 s38, s36, 0x2000
	s_addc_u32 s39, s37, 0
	s_sub_i32 s2, s47, 4
	v_cmp_gt_i32_e32 vcc, s2, v79
	s_and_saveexec_b64 s[48:49], vcc
	global_store_dwordx4 v73, v[104:107], s[38:39]
	s_mov_b64 exec, s[48:49]
	s_add_u32 s38, s36, 0x4000
	s_addc_u32 s39, s37, 0
	s_sub_i32 s2, s47, 8
	v_cmp_gt_i32_e32 vcc, s2, v79
	s_and_saveexec_b64 s[48:49], vcc
	global_store_dwordx4 v73, v[108:111], s[38:39]
	s_mov_b64 exec, s[48:49]
	s_add_u32 s38, s36, 0x6000
	s_addc_u32 s39, s37, 0
	s_sub_i32 s2, s47, 12
	v_cmp_gt_i32_e32 vcc, s2, v79
	s_and_saveexec_b64 s[48:49], vcc
	global_store_dwordx4 v73, v[112:115], s[38:39]
	s_mov_b64 exec, s[48:49]
	v_fmamk_f32 v46, v46, 0x35800000, v74
	v_fmamk_f32 v47, v47, 0x35800000, v74
	v_fmamk_f32 v48, v48, 0x35800000, v74
	v_fmamk_f32 v49, v49, 0x35800000, v74
	v_fmamk_f32 v42, v42, 0x35800000, v75
	v_fmamk_f32 v43, v43, 0x35800000, v75
	v_fmamk_f32 v44, v44, 0x35800000, v75
	v_fmamk_f32 v45, v45, 0x35800000, v75
	v_fmamk_f32 v38, v38, 0x35800000, v76
	v_fmamk_f32 v39, v39, 0x35800000, v76
	v_fmamk_f32 v40, v40, 0x35800000, v76
	v_fmamk_f32 v41, v41, 0x35800000, v76
	v_fmamk_f32 v34, v34, 0x35800000, v77
	v_fmamk_f32 v35, v35, 0x35800000, v77
	v_fmamk_f32 v36, v36, 0x35800000, v77
	v_fmamk_f32 v37, v37, 0x35800000, v77
	v_mul_f32_e32 v46, v46, v88
	v_mul_f32_e32 v47, v47, v89
	v_mul_f32_e32 v48, v48, v90
	v_mul_f32_e32 v49, v49, v91
	v_mul_f32_e32 v42, v42, v88
	v_mul_f32_e32 v43, v43, v89
	v_mul_f32_e32 v44, v44, v90
	v_mul_f32_e32 v45, v45, v91
	v_mul_f32_e32 v38, v38, v88
	v_mul_f32_e32 v39, v39, v89
	v_mul_f32_e32 v40, v40, v90
	v_mul_f32_e32 v41, v41, v91
	v_mul_f32_e32 v34, v34, v88
	v_mul_f32_e32 v35, v35, v89
	v_mul_f32_e32 v36, v36, v90
	v_mul_f32_e32 v37, v37, v91
	ds_write_b32 v71, v46
	ds_write_b32 v71, v47 offset:272
	ds_write_b32 v71, v48 offset:544
	ds_write_b32 v71, v49 offset:816
	ds_write_b32 v71, v42 offset:64
	ds_write_b32 v71, v43 offset:336
	ds_write_b32 v71, v44 offset:608
	ds_write_b32 v71, v45 offset:880
	ds_write_b32 v71, v38 offset:128
	ds_write_b32 v71, v39 offset:400
	ds_write_b32 v71, v40 offset:672
	ds_write_b32 v71, v41 offset:944
	ds_write_b32 v71, v34 offset:192
	ds_write_b32 v71, v35 offset:464
	ds_write_b32 v71, v36 offset:736
	ds_write_b32 v71, v37 offset:1008
	ds_read_b128 v[116:119], v78
	ds_read_b128 v[120:123], v78 offset:1088
	ds_read_b128 v[124:127], v78 offset:2176
	ds_read_b128 v[128:131], v78 offset:3264
	s_waitcnt lgkmcnt(0)
	s_add_u32 s38, s36, 0x8000
	s_addc_u32 s39, s37, 0
	s_sub_i32 s2, s47, 16
	v_cmp_gt_i32_e32 vcc, s2, v79
	s_and_saveexec_b64 s[48:49], vcc
	global_store_dwordx4 v73, v[116:119], s[38:39]
	s_mov_b64 exec, s[48:49]
	s_add_u32 s38, s36, 0xa000
	s_addc_u32 s39, s37, 0
	s_sub_i32 s2, s47, 20
	v_cmp_gt_i32_e32 vcc, s2, v79
	s_and_saveexec_b64 s[48:49], vcc
	global_store_dwordx4 v73, v[120:123], s[38:39]
	s_mov_b64 exec, s[48:49]
	s_add_u32 s38, s36, 0xc000
	s_addc_u32 s39, s37, 0
	s_sub_i32 s2, s47, 24
	v_cmp_gt_i32_e32 vcc, s2, v79
	s_and_saveexec_b64 s[48:49], vcc
	global_store_dwordx4 v73, v[124:127], s[38:39]
	s_mov_b64 exec, s[48:49]
	s_add_u32 s38, s36, 0xe000
	s_addc_u32 s39, s37, 0
	s_sub_i32 s2, s47, 28
	v_cmp_gt_i32_e32 vcc, s2, v79
	s_and_saveexec_b64 s[48:49], vcc
	global_store_dwordx4 v73, v[128:131], s[38:39]
	s_mov_b64 exec, s[48:49]
	v_fmamk_f32 v30, v30, 0x35800000, v74
	v_fmamk_f32 v31, v31, 0x35800000, v74
	v_fmamk_f32 v32, v32, 0x35800000, v74
	v_fmamk_f32 v33, v33, 0x35800000, v74
	v_fmamk_f32 v26, v26, 0x35800000, v75
	v_fmamk_f32 v27, v27, 0x35800000, v75
	v_fmamk_f32 v28, v28, 0x35800000, v75
	v_fmamk_f32 v29, v29, 0x35800000, v75
	v_fmamk_f32 v22, v22, 0x35800000, v76
	v_fmamk_f32 v23, v23, 0x35800000, v76
	v_fmamk_f32 v24, v24, 0x35800000, v76
	v_fmamk_f32 v25, v25, 0x35800000, v76
	v_fmamk_f32 v18, v18, 0x35800000, v77
	v_fmamk_f32 v19, v19, 0x35800000, v77
	v_fmamk_f32 v20, v20, 0x35800000, v77
	v_fmamk_f32 v21, v21, 0x35800000, v77
	v_mul_f32_e32 v30, v30, v92
	v_mul_f32_e32 v31, v31, v93
	v_mul_f32_e32 v32, v32, v94
	v_mul_f32_e32 v33, v33, v95
	v_mul_f32_e32 v26, v26, v92
	v_mul_f32_e32 v27, v27, v93
	v_mul_f32_e32 v28, v28, v94
	v_mul_f32_e32 v29, v29, v95
	v_mul_f32_e32 v22, v22, v92
	v_mul_f32_e32 v23, v23, v93
	v_mul_f32_e32 v24, v24, v94
	v_mul_f32_e32 v25, v25, v95
	v_mul_f32_e32 v18, v18, v92
	v_mul_f32_e32 v19, v19, v93
	v_mul_f32_e32 v20, v20, v94
	v_mul_f32_e32 v21, v21, v95
	ds_write_b32 v71, v30
	ds_write_b32 v71, v31 offset:272
	ds_write_b32 v71, v32 offset:544
	ds_write_b32 v71, v33 offset:816
	ds_write_b32 v71, v26 offset:64
	ds_write_b32 v71, v27 offset:336
	ds_write_b32 v71, v28 offset:608
	ds_write_b32 v71, v29 offset:880
	ds_write_b32 v71, v22 offset:128
	ds_write_b32 v71, v23 offset:400
	ds_write_b32 v71, v24 offset:672
	ds_write_b32 v71, v25 offset:944
	ds_write_b32 v71, v18 offset:192
	ds_write_b32 v71, v19 offset:464
	ds_write_b32 v71, v20 offset:736
	ds_write_b32 v71, v21 offset:1008
	ds_read_b128 v[100:103], v78
	ds_read_b128 v[104:107], v78 offset:1088
	ds_read_b128 v[108:111], v78 offset:2176
	ds_read_b128 v[112:115], v78 offset:3264
	s_waitcnt lgkmcnt(0)
	s_add_u32 s38, s36, 0x10000
	s_addc_u32 s39, s37, 0
	s_sub_i32 s2, s47, 32
	v_cmp_gt_i32_e32 vcc, s2, v79
	s_and_saveexec_b64 s[48:49], vcc
	global_store_dwordx4 v73, v[100:103], s[38:39]
	s_mov_b64 exec, s[48:49]
	s_add_u32 s38, s36, 0x12000
	s_addc_u32 s39, s37, 0
	s_sub_i32 s2, s47, 36
	v_cmp_gt_i32_e32 vcc, s2, v79
	s_and_saveexec_b64 s[48:49], vcc
	global_store_dwordx4 v73, v[104:107], s[38:39]
	s_mov_b64 exec, s[48:49]
	s_add_u32 s38, s36, 0x14000
	s_addc_u32 s39, s37, 0
	s_sub_i32 s2, s47, 40
	v_cmp_gt_i32_e32 vcc, s2, v79
	s_and_saveexec_b64 s[48:49], vcc
	global_store_dwordx4 v73, v[108:111], s[38:39]
	s_mov_b64 exec, s[48:49]
	s_add_u32 s38, s36, 0x16000
	s_addc_u32 s39, s37, 0
	s_sub_i32 s2, s47, 44
	v_cmp_gt_i32_e32 vcc, s2, v79
	s_and_saveexec_b64 s[48:49], vcc
	global_store_dwordx4 v73, v[112:115], s[38:39]
	s_mov_b64 exec, s[48:49]
	v_fmamk_f32 v14, v14, 0x35800000, v74
	v_fmamk_f32 v15, v15, 0x35800000, v74
	v_fmamk_f32 v16, v16, 0x35800000, v74
	v_fmamk_f32 v17, v17, 0x35800000, v74
	v_fmamk_f32 v10, v10, 0x35800000, v75
	v_fmamk_f32 v11, v11, 0x35800000, v75
	v_fmamk_f32 v12, v12, 0x35800000, v75
	v_fmamk_f32 v13, v13, 0x35800000, v75
	v_fmamk_f32 v6, v6, 0x35800000, v76
	v_fmamk_f32 v7, v7, 0x35800000, v76
	v_fmamk_f32 v8, v8, 0x35800000, v76
	v_fmamk_f32 v9, v9, 0x35800000, v76
	v_fmamk_f32 v2, v2, 0x35800000, v77
	v_fmamk_f32 v3, v3, 0x35800000, v77
	v_fmamk_f32 v4, v4, 0x35800000, v77
	v_fmamk_f32 v5, v5, 0x35800000, v77
	v_mul_f32_e32 v14, v14, v96
	v_mul_f32_e32 v15, v15, v97
	v_mul_f32_e32 v16, v16, v98
	v_mul_f32_e32 v17, v17, v99
	v_mul_f32_e32 v10, v10, v96
	v_mul_f32_e32 v11, v11, v97
	v_mul_f32_e32 v12, v12, v98
	v_mul_f32_e32 v13, v13, v99
	v_mul_f32_e32 v6, v6, v96
	v_mul_f32_e32 v7, v7, v97
	v_mul_f32_e32 v8, v8, v98
	v_mul_f32_e32 v9, v9, v99
	v_mul_f32_e32 v2, v2, v96
	v_mul_f32_e32 v3, v3, v97
	v_mul_f32_e32 v4, v4, v98
	v_mul_f32_e32 v5, v5, v99
	ds_write_b32 v71, v14
	ds_write_b32 v71, v15 offset:272
	ds_write_b32 v71, v16 offset:544
	ds_write_b32 v71, v17 offset:816
	ds_write_b32 v71, v10 offset:64
	ds_write_b32 v71, v11 offset:336
	ds_write_b32 v71, v12 offset:608
	ds_write_b32 v71, v13 offset:880
	ds_write_b32 v71, v6 offset:128
	ds_write_b32 v71, v7 offset:400
	ds_write_b32 v71, v8 offset:672
	ds_write_b32 v71, v9 offset:944
	ds_write_b32 v71, v2 offset:192
	ds_write_b32 v71, v3 offset:464
	ds_write_b32 v71, v4 offset:736
	ds_write_b32 v71, v5 offset:1008
	ds_read_b128 v[116:119], v78
	ds_read_b128 v[120:123], v78 offset:1088
	ds_read_b128 v[124:127], v78 offset:2176
	ds_read_b128 v[128:131], v78 offset:3264
	s_waitcnt lgkmcnt(0)
	s_add_u32 s38, s36, 0x18000
	s_addc_u32 s39, s37, 0
	s_sub_i32 s2, s47, 48
	v_cmp_gt_i32_e32 vcc, s2, v79
	s_and_saveexec_b64 s[48:49], vcc
	global_store_dwordx4 v73, v[116:119], s[38:39]
	s_mov_b64 exec, s[48:49]
	s_add_u32 s38, s36, 0x1a000
	s_addc_u32 s39, s37, 0
	s_sub_i32 s2, s47, 52
	v_cmp_gt_i32_e32 vcc, s2, v79
	s_and_saveexec_b64 s[48:49], vcc
	global_store_dwordx4 v73, v[120:123], s[38:39]
	s_mov_b64 exec, s[48:49]
	s_add_u32 s38, s36, 0x1c000
	s_addc_u32 s39, s37, 0
	s_sub_i32 s2, s47, 56
	v_cmp_gt_i32_e32 vcc, s2, v79
	s_and_saveexec_b64 s[48:49], vcc
	global_store_dwordx4 v73, v[124:127], s[38:39]
	s_mov_b64 exec, s[48:49]
	s_add_u32 s38, s36, 0x1e000
	s_addc_u32 s39, s37, 0
	s_sub_i32 s2, s47, 60
	v_cmp_gt_i32_e32 vcc, s2, v79
	s_and_saveexec_b64 s[48:49], vcc
	global_store_dwordx4 v73, v[128:131], s[38:39]
	s_mov_b64 exec, s[48:49]
	s_endpgm

	.amdhsa_kernel _Z13gemm64_kernelILi1ELi3ELb1ELi1EEv2GP
		.amdhsa_group_segment_fixed_size 32768
		.amdhsa_private_segment_fixed_size 0
		.amdhsa_kernarg_size 440
		.amdhsa_user_sgpr_count 2
		.amdhsa_user_sgpr_dispatch_ptr 0
		.amdhsa_user_sgpr_queue_ptr 0
		.amdhsa_user_sgpr_kernarg_segment_ptr 1
		.amdhsa_user_sgpr_dispatch_id 0
		.amdhsa_user_sgpr_kernarg_preload_length 0
		.amdhsa_user_sgpr_kernarg_preload_offset 0
		.amdhsa_user_sgpr_private_segment_size 0
		.amdhsa_uses_dynamic_stack 0
		.amdhsa_enable_private_segment 0
		.amdhsa_system_sgpr_workgroup_id_x 1
		.amdhsa_system_sgpr_workgroup_id_y 1
		.amdhsa_system_sgpr_workgroup_id_z 0
		.amdhsa_system_sgpr_workgroup_info 0
		.amdhsa_system_vgpr_workitem_id 0
		.amdhsa_next_free_vgpr 132
		.amdhsa_next_free_sgpr 96
		.amdhsa_accum_offset 132
		.amdhsa_reserve_vcc 1
		.amdhsa_float_round_mode_32 0
		.amdhsa_float_round_mode_16_64 0
		.amdhsa_float_denorm_mode_32 3
		.amdhsa_float_denorm_mode_16_64 3
		.amdhsa_dx10_clamp 1
		.amdhsa_ieee_mode 1
		.amdhsa_fp16_overflow 0
		.amdhsa_tg_split 0
		.amdhsa_exception_fp_ieee_invalid_op 0
		.amdhsa_exception_fp_denorm_src 0
		.amdhsa_exception_fp_ieee_div_zero 0
		.amdhsa_exception_fp_ieee_overflow 0
		.amdhsa_exception_fp_ieee_underflow 0
		.amdhsa_exception_fp_ieee_inexact 0
		.amdhsa_exception_int_div_zero 0
	.end_amdhsa_kernel
